# baseline (speedup 1.0000x reference)
.LBB1_8:
	s_or_b64 exec, exec, s[8:9]
	v_mul_f32_e32 v131, 0x42c80000, v178
	s_mov_b32 s0, 0x24400
	s_mov_b32 s8, 0x3a000000
	s_lshl_b32 s11, s2, 9
	v_min3_f32 v130, v131, v130, 1.0
	v_or3_b32 v218, v162, v163, s0
	v_mov_b32_e32 v177, 0
	s_mov_b64 s[22:23], 0
	s_mov_b32 s0, 0
	s_mov_b32 s15, 0x45000000
	s_mov_b32 s9, 0x34800000
	s_mov_b32 s17, 0x3f7a4fa5
	s_mov_b32 s19, 0x403cf760
	s_mov_b32 s21, 0x40362960
	s_mov_b32 s10, 0x3dbaaaab
	s_mov_b32 s14, 0x3ee6024d
	s_mov_b32 s16, 0x3f26aaab
	s_mov_b32 s18, 0x3ea50e7e
	s_mov_b32 s20, 0x3e061862
	s_mov_b32 s28, 0x3aa1907f
	v_mov_b32_e32 v219, 0x358637bd
	v_mov_b32_e32 v220, 0x41200000
	s_mov_b32 s29, 0
	s_mov_b32 s30, 0
	v_mov_b32_e32 v221, 0
	s_waitcnt vmcnt(0) lgkmcnt(0)
	v_mov_b32_e32 v1, v130
	s_mov_b32 s40, 0x3a000000
	s_mov_b32 s41, 0x34800000
	s_mov_b32 s42, 0x45000000
	v_mul_f32_e32 v173, 0x44000000, v173
	v_mul_f32_e32 v172, 0x44000000, v172
	v_mul_f32_e32 v175, 0x44000000, v175
	v_mul_f32_e32 v174, 0x44000000, v174
	v_mov_b64_e32 v[230:231], 0
	v_mov_b64_e32 v[232:233], 0
	v_mov_b64_e32 v[234:235], 0
	v_mov_b64_e32 v[236:237], 0
.Lrk_top:
	v_sub_f32_e32 v238, 1.0, v221
	v_min_f32_e32 v178, v1, v238
	v_cmp_eq_f32_e32 vcc, 0, v178
	v_mul_f32_e32 v178, 0x3b000000, v178
	s_cmp_eq_u64 vcc, exec
	s_cbranch_scc1 .Lrk_exit
	s_cmp_gt_i32 s30, 63
	s_cbranch_scc1 .Lrk_exit
	v_mul_f32_e32 v134, 0x3e4ccccd, v173
	v_mul_f32_e32 v142, 0x3e4ccccd, v172
	v_mul_f32_e32 v150, 0x3e4ccccd, v175
	v_mul_f32_e32 v158, 0x3e4ccccd, v174
	v_fma_mixlo_f16 v131, v178, v134, v171
	v_fma_mixlo_f16 v139, v178, v142, v170
	v_fma_mixlo_f16 v147, v178, v150, v169
	v_fma_mixlo_f16 v155, v178, v158, v168
	v_fma_f32 v130, v178, v134, v171
	v_fma_f32 v138, v178, v142, v170
	v_fma_f32 v146, v178, v150, v169
	v_fma_f32 v154, v178, v158, v168
	v_fma_mix_f32 v130, v130, 1.0, -v131 op_sel_hi:[0,0,1]
	v_fma_mix_f32 v138, v138, 1.0, -v139 op_sel_hi:[0,0,1]
	v_fma_mix_f32 v146, v146, 1.0, -v147 op_sel_hi:[0,0,1]
	v_fma_mix_f32 v154, v154, 1.0, -v155 op_sel_hi:[0,0,1]
	v_fma_mixlo_f16 v133, v130, s42, 0
	v_fma_mixlo_f16 v141, v138, s42, 0
	v_fma_mixlo_f16 v149, v146, s42, 0
	v_fma_mixlo_f16 v157, v154, s42, 0
	v_fma_mix_f32 v130, v130, s42, -v133 op_sel_hi:[0,0,1]
	v_fma_mix_f32 v138, v138, s42, -v141 op_sel_hi:[0,0,1]
	v_fma_mix_f32 v146, v146, s42, -v149 op_sel_hi:[0,0,1]
	v_fma_mix_f32 v154, v154, s42, -v157 op_sel_hi:[0,0,1]
	v_fma_mixlo_f16 v132, v130, s42, 0
	v_fma_mixlo_f16 v140, v138, s42, 0
	v_fma_mixlo_f16 v148, v146, s42, 0
	v_fma_mixlo_f16 v156, v154, s42, 0
	ds_write_b16 v204, v131
	ds_write_b16 v205, v139
	ds_write_b16 v206, v147
	ds_write_b16 v207, v155
	ds_write_b16 v204, v133 offset:544
	ds_write_b16 v205, v141 offset:544
	ds_write_b16 v206, v149 offset:544
	ds_write_b16 v207, v157 offset:544
	ds_write_b16 v204, v132 offset:1088
	ds_write_b16 v205, v140 offset:1088
	ds_write_b16 v206, v148 offset:1088
	ds_write_b16 v207, v156 offset:1088
	s_waitcnt lgkmcnt(0)
	s_barrier
	ds_read_b128 v[130:133], v208
	ds_read_b128 v[134:137], v209 offset:64
	ds_read_b128 v[138:141], v211
	ds_read_b128 v[142:145], v212
	ds_read_b128 v[146:149], v213
	ds_read_b128 v[150:153], v214
	ds_read_b128 v[154:157], v215
	ds_read_b128 v[158:161], v216
	ds_read_b128 v[180:183], v199 offset:0
	ds_read_b128 v[184:187], v199 offset:1024
	ds_read_b128 v[188:191], v199 offset:4096
	ds_read_b128 v[192:195], v199 offset:5120
	ds_read_b128 v[222:225], v199 offset:8192
	ds_read_b128 v[226:229], v199 offset:9216
	s_waitcnt lgkmcnt(13)
	v_smfmac_f32_16x16x64_f16 v[230:233], v[130:133], a[0:7], v210
	v_mov_b64_e32 v[238:239], 0
	v_mov_b64_e32 v[240:241], 0
	v_smfmac_f32_16x16x64_f16 v[234:237], v[130:133], v[18:25], v210
	v_mov_b64_e32 v[242:243], 0
	v_mov_b64_e32 v[244:245], 0
	s_waitcnt lgkmcnt(12)
	v_smfmac_f32_16x16x64_f16 v[230:233], v[134:137], a[40:47], v210
	v_mul_f32_e32 v166, 0x3d99999a, v173
	v_mul_f32_e32 v167, 0x3d99999a, v172
	v_smfmac_f32_16x16x64_f16 v[234:237], v[134:137], v[34:41], v210
	v_mul_f32_e32 v176, 0x3d99999a, v175
	v_mul_f32_e32 v177, 0x3d99999a, v174
	s_waitcnt lgkmcnt(11)
	v_smfmac_f32_16x16x64_f16 v[230:233], v[138:141], a[64:71], v210
	v_smfmac_f32_16x16x64_f16 v[234:237], v[138:141], v[42:49], v210
	s_waitcnt lgkmcnt(10)
	v_smfmac_f32_16x16x64_f16 v[230:233], v[142:145], a[96:103], v210
	v_smfmac_f32_16x16x64_f16 v[234:237], v[142:145], v[58:65], v210
	s_waitcnt lgkmcnt(9)
	v_smfmac_f32_16x16x64_f16 v[230:233], v[146:149], a[128:135], v210
	v_smfmac_f32_16x16x64_f16 v[234:237], v[146:149], v[74:81], v210
	s_waitcnt lgkmcnt(8)
	v_smfmac_f32_16x16x64_f16 v[230:233], v[150:153], a[160:167], v210
	v_smfmac_f32_16x16x64_f16 v[234:237], v[150:153], v[98:105], v210
	s_waitcnt lgkmcnt(7)
	v_smfmac_f32_16x16x64_f16 v[230:233], v[154:157], a[192:199], v210
	v_smfmac_f32_16x16x64_f16 v[234:237], v[154:157], v[106:113], v210
	s_waitcnt lgkmcnt(6)
	v_smfmac_f32_16x16x64_f16 v[230:233], v[158:161], a[224:231], v210
	v_smfmac_f32_16x16x64_f16 v[234:237], v[158:161], v[122:129], v210
	v_smfmac_f32_16x16x64_f16 v[238:241], v[130:133], a[16:23], v210
	s_waitcnt lgkmcnt(4)
	v_smfmac_f32_16x16x64_f16 v[242:245], v[130:133], v[180:187], v210
	ds_read_b128 v[180:183], v199 offset:12288
	ds_read_b128 v[184:187], v199 offset:13312
	v_smfmac_f32_16x16x64_f16 v[238:241], v[134:137], a[48:55], v210
	v_fmac_f32_e32 v230, s40, v231
	v_fmac_f32_e32 v234, s40, v235
	s_waitcnt lgkmcnt(4)
	v_smfmac_f32_16x16x64_f16 v[242:245], v[134:137], v[188:195], v210
	ds_read_b128 v[188:191], v199 offset:16384
	ds_read_b128 v[192:195], v199 offset:17408
	v_fmac_f32_e32 v230, s41, v232
	v_fmac_f32_e32 v234, s41, v236
	v_smfmac_f32_16x16x64_f16 v[238:241], v[138:141], a[80:87], v210
	s_nop 0
	v_permlane32_swap_b32_e32 v230, v234
	v_add_f32_e32 v162, v230, v234
	s_waitcnt lgkmcnt(4)
	v_smfmac_f32_16x16x64_f16 v[242:245], v[138:141], v[222:229], v210
	ds_read_b128 v[222:225], v199 offset:20480
	ds_read_b128 v[226:229], v199 offset:21504
	v_fmac_f32_e32 v166, 0x3e666666, v162
	v_fma_mixlo_f16 v232, v178, v166, v171
	v_smfmac_f32_16x16x64_f16 v[238:241], v[142:145], a[112:119], v210
	v_fma_f32 v231, v178, v166, v171
	v_fma_mix_f32 v231, v231, 1.0, -v232 op_sel_hi:[0,0,1]
	s_waitcnt lgkmcnt(4)
	v_smfmac_f32_16x16x64_f16 v[242:245], v[142:145], v[180:187], v210
	ds_read_b128 v[180:183], v199 offset:24576
	ds_read_b128 v[184:187], v199 offset:25600
	v_fma_mixlo_f16 v235, v231, s42, 0
	v_fma_mix_f32 v231, v231, s42, -v235 op_sel_hi:[0,0,1]
	v_smfmac_f32_16x16x64_f16 v[238:241], v[146:149], a[144:151], v210
	v_fma_mixlo_f16 v233, v231, s42, 0
	ds_write_b16 v204, v232 offset:8704
	s_waitcnt lgkmcnt(5)
	v_smfmac_f32_16x16x64_f16 v[242:245], v[146:149], v[188:195], v210
	ds_read_b128 v[188:191], v199 offset:28672
	ds_read_b128 v[192:195], v199 offset:29696
	ds_write_b16 v204, v235 offset:9248
	ds_write_b16 v204, v233 offset:9792
	v_smfmac_f32_16x16x64_f16 v[238:241], v[150:153], a[176:183], v210
	v_mov_b64_e32 v[230:231], 0
	v_mov_b64_e32 v[232:233], 0
	s_waitcnt lgkmcnt(7)
	v_smfmac_f32_16x16x64_f16 v[242:245], v[150:153], v[222:229], v210
	ds_read_b128 v[222:225], v199 offset:2048
	ds_read_b128 v[226:229], v199 offset:3072
	v_mov_b64_e32 v[234:235], 0
	v_mov_b64_e32 v[236:237], 0
	v_smfmac_f32_16x16x64_f16 v[238:241], v[154:157], a[208:215], v210
	s_waitcnt lgkmcnt(7)
	v_smfmac_f32_16x16x64_f16 v[242:245], v[154:157], v[180:187], v210
	ds_read_b128 v[180:183], v199 offset:6144
	ds_read_b128 v[184:187], v199 offset:7168
	v_smfmac_f32_16x16x64_f16 v[238:241], v[158:161], a[240:247], v210
	s_waitcnt lgkmcnt(6)
	v_smfmac_f32_16x16x64_f16 v[242:245], v[158:161], v[188:195], v210
	ds_read_b128 v[188:191], v199 offset:10240
	ds_read_b128 v[192:195], v199 offset:11264
	v_smfmac_f32_16x16x64_f16 v[230:233], v[130:133], a[8:15], v210
	v_smfmac_f32_16x16x64_f16 v[234:237], v[130:133], v[2:9], v210
	v_smfmac_f32_16x16x64_f16 v[230:233], v[134:137], a[32:39], v210
	v_fmac_f32_e32 v238, s40, v239
	v_fmac_f32_e32 v242, s40, v243
	v_smfmac_f32_16x16x64_f16 v[234:237], v[134:137], v[10:17], v210
	v_fmac_f32_e32 v238, s41, v240
	v_fmac_f32_e32 v242, s41, v244
	v_smfmac_f32_16x16x64_f16 v[230:233], v[138:141], a[72:79], v210
	s_nop 0
	v_permlane32_swap_b32_e32 v238, v242
	v_add_f32_e32 v164, v238, v242
	v_smfmac_f32_16x16x64_f16 v[234:237], v[138:141], v[50:57], v210
	v_fmac_f32_e32 v176, 0x3e666666, v164
	v_fma_mixlo_f16 v240, v178, v176, v169
	v_smfmac_f32_16x16x64_f16 v[230:233], v[142:145], a[104:111], v210
	v_fma_f32 v239, v178, v176, v169
	v_fma_mix_f32 v239, v239, 1.0, -v240 op_sel_hi:[0,0,1]
	v_smfmac_f32_16x16x64_f16 v[234:237], v[142:145], v[26:33], v210
	v_fma_mixlo_f16 v243, v239, s42, 0
	v_fma_mix_f32 v239, v239, s42, -v243 op_sel_hi:[0,0,1]
	v_smfmac_f32_16x16x64_f16 v[230:233], v[146:149], a[136:143], v210
	v_fma_mixlo_f16 v241, v239, s42, 0
	ds_write_b16 v206, v240 offset:8704
	v_smfmac_f32_16x16x64_f16 v[234:237], v[146:149], v[82:89], v210
	ds_write_b16 v206, v243 offset:9248
	ds_write_b16 v206, v241 offset:9792
	v_smfmac_f32_16x16x64_f16 v[230:233], v[150:153], a[168:175], v210
	v_mov_b64_e32 v[238:239], 0
	v_mov_b64_e32 v[240:241], 0
	v_smfmac_f32_16x16x64_f16 v[234:237], v[150:153], v[66:73], v210
	v_mov_b64_e32 v[242:243], 0
	v_mov_b64_e32 v[244:245], 0
	v_smfmac_f32_16x16x64_f16 v[230:233], v[154:157], a[200:207], v210
	v_smfmac_f32_16x16x64_f16 v[234:237], v[154:157], v[114:121], v210
	v_smfmac_f32_16x16x64_f16 v[230:233], v[158:161], a[232:239], v210
	v_smfmac_f32_16x16x64_f16 v[234:237], v[158:161], v[90:97], v210
	v_smfmac_f32_16x16x64_f16 v[238:241], v[130:133], a[24:31], v210
	s_waitcnt lgkmcnt(7)
	v_smfmac_f32_16x16x64_f16 v[242:245], v[130:133], v[222:229], v210
	ds_read_b128 v[222:225], v199 offset:14336
	ds_read_b128 v[226:229], v199 offset:15360
	v_smfmac_f32_16x16x64_f16 v[238:241], v[134:137], a[56:63], v210
	v_fmac_f32_e32 v230, s40, v231
	v_fmac_f32_e32 v234, s40, v235
	s_waitcnt lgkmcnt(7)
	v_smfmac_f32_16x16x64_f16 v[242:245], v[134:137], v[180:187], v210
	ds_read_b128 v[180:183], v199 offset:18432
	ds_read_b128 v[184:187], v199 offset:19456
	v_fmac_f32_e32 v230, s41, v232
	v_fmac_f32_e32 v234, s41, v236
	v_smfmac_f32_16x16x64_f16 v[238:241], v[138:141], a[88:95], v210
	s_nop 0
	v_permlane32_swap_b32_e32 v230, v234
	v_add_f32_e32 v163, v230, v234
	s_waitcnt lgkmcnt(7)
	v_smfmac_f32_16x16x64_f16 v[242:245], v[138:141], v[188:195], v210
	ds_read_b128 v[188:191], v199 offset:22528
	ds_read_b128 v[192:195], v199 offset:23552
	v_fmac_f32_e32 v167, 0x3e666666, v163
	v_fma_mixlo_f16 v232, v178, v167, v170
	v_smfmac_f32_16x16x64_f16 v[238:241], v[142:145], a[120:127], v210
	v_fma_f32 v231, v178, v167, v170
	v_fma_mix_f32 v231, v231, 1.0, -v232 op_sel_hi:[0,0,1]
	s_waitcnt lgkmcnt(4)
	v_smfmac_f32_16x16x64_f16 v[242:245], v[142:145], v[222:229], v210
	ds_read_b128 v[222:225], v199 offset:26624
	ds_read_b128 v[226:229], v199 offset:27648
	v_fma_mixlo_f16 v235, v231, s42, 0
	v_fma_mix_f32 v231, v231, s42, -v235 op_sel_hi:[0,0,1]
	v_smfmac_f32_16x16x64_f16 v[238:241], v[146:149], a[152:159], v210
	v_fma_mixlo_f16 v233, v231, s42, 0
	ds_write_b16 v205, v232 offset:8704
	s_waitcnt lgkmcnt(5)
	v_smfmac_f32_16x16x64_f16 v[242:245], v[146:149], v[180:187], v210
	ds_read_b128 v[180:183], v199 offset:30720
	ds_read_b128 v[184:187], v199 offset:31744
	ds_write_b16 v205, v235 offset:9248
	ds_write_b16 v205, v233 offset:9792
	v_smfmac_f32_16x16x64_f16 v[238:241], v[150:153], a[184:191], v210
	v_mov_b64_e32 v[230:231], 0
	v_mov_b64_e32 v[232:233], 0
	s_waitcnt lgkmcnt(7)
	v_smfmac_f32_16x16x64_f16 v[242:245], v[150:153], v[188:195], v210
	v_mov_b64_e32 v[234:235], 0
	v_mov_b64_e32 v[236:237], 0
	v_smfmac_f32_16x16x64_f16 v[238:241], v[154:157], a[216:223], v210
	s_waitcnt lgkmcnt(5)
	v_smfmac_f32_16x16x64_f16 v[242:245], v[154:157], v[222:229], v210
	v_smfmac_f32_16x16x64_f16 v[238:241], v[158:161], a[248:255], v210
	s_waitcnt lgkmcnt(2)
	v_smfmac_f32_16x16x64_f16 v[242:245], v[158:161], v[180:187], v210
	s_nop 5
	v_fmac_f32_e32 v238, s40, v239
	s_nop 0
	v_fmac_f32_e32 v242, s40, v243
	v_fmac_f32_e32 v238, s41, v240
	v_fmac_f32_e32 v242, s41, v244
	s_nop 1
	v_permlane32_swap_b32_e32 v238, v242
	v_add_f32_e32 v165, v238, v242
	v_fmac_f32_e32 v177, 0x3e666666, v165
	v_fma_mixlo_f16 v240, v178, v177, v168
	v_fma_f32 v239, v178, v177, v168
	v_fma_mix_f32 v239, v239, 1.0, -v240 op_sel_hi:[0,0,1]
	v_fma_mixlo_f16 v243, v239, s42, 0
	v_fma_mix_f32 v239, v239, s42, -v243 op_sel_hi:[0,0,1]
	v_fma_mixlo_f16 v241, v239, s42, 0
	ds_write_b16 v207, v240 offset:8704
	ds_write_b16 v207, v243 offset:9248
	ds_write_b16 v207, v241 offset:9792
	s_waitcnt lgkmcnt(0)
	s_barrier
	ds_read_b128 v[130:133], v208 offset:8704
	ds_read_b128 v[134:137], v209 offset:8768
	ds_read_b128 v[138:141], v211 offset:8704
	ds_read_b128 v[142:145], v212 offset:8704
	ds_read_b128 v[146:149], v213 offset:8704
	ds_read_b128 v[150:153], v214 offset:8704
	ds_read_b128 v[154:157], v215 offset:8704
	ds_read_b128 v[158:161], v216 offset:8704
	ds_read_b128 v[180:183], v199 offset:0
	ds_read_b128 v[184:187], v199 offset:1024
	ds_read_b128 v[188:191], v199 offset:4096
	ds_read_b128 v[192:195], v199 offset:5120
	ds_read_b128 v[222:225], v199 offset:8192
	ds_read_b128 v[226:229], v199 offset:9216
	s_waitcnt lgkmcnt(13)
	v_smfmac_f32_16x16x64_f16 v[230:233], v[130:133], a[0:7], v210
	v_mov_b64_e32 v[238:239], 0
	v_mov_b64_e32 v[240:241], 0
	v_smfmac_f32_16x16x64_f16 v[234:237], v[130:133], v[18:25], v210
	v_mov_b64_e32 v[242:243], 0
	v_mov_b64_e32 v[244:245], 0
	s_waitcnt lgkmcnt(12)
	v_smfmac_f32_16x16x64_f16 v[230:233], v[134:137], a[40:47], v210
	v_mul_f32_e32 v179, 0x3f7a4fa5, v173
	v_fmac_f32_e32 v179, 0xc06eeeef, v162
	v_smfmac_f32_16x16x64_f16 v[234:237], v[134:137], v[34:41], v210
	v_mul_f32_e32 v196, 0x3f7a4fa5, v172
	v_fmac_f32_e32 v196, 0xc06eeeef, v163
	s_waitcnt lgkmcnt(11)
	v_smfmac_f32_16x16x64_f16 v[230:233], v[138:141], a[64:71], v210
	v_mul_f32_e32 v197, 0x3f7a4fa5, v175
	v_fmac_f32_e32 v197, 0xc06eeeef, v164
	v_smfmac_f32_16x16x64_f16 v[234:237], v[138:141], v[42:49], v210
	v_mul_f32_e32 v198, 0x3f7a4fa5, v174
	v_fmac_f32_e32 v198, 0xc06eeeef, v165
	s_waitcnt lgkmcnt(10)
	v_smfmac_f32_16x16x64_f16 v[230:233], v[142:145], a[96:103], v210
	v_smfmac_f32_16x16x64_f16 v[234:237], v[142:145], v[58:65], v210
	s_waitcnt lgkmcnt(9)
	v_smfmac_f32_16x16x64_f16 v[230:233], v[146:149], a[128:135], v210
	v_smfmac_f32_16x16x64_f16 v[234:237], v[146:149], v[74:81], v210
	s_waitcnt lgkmcnt(8)
	v_smfmac_f32_16x16x64_f16 v[230:233], v[150:153], a[160:167], v210
	v_smfmac_f32_16x16x64_f16 v[234:237], v[150:153], v[98:105], v210
	s_waitcnt lgkmcnt(7)
	v_smfmac_f32_16x16x64_f16 v[230:233], v[154:157], a[192:199], v210
	v_smfmac_f32_16x16x64_f16 v[234:237], v[154:157], v[106:113], v210
	s_waitcnt lgkmcnt(6)
	v_smfmac_f32_16x16x64_f16 v[230:233], v[158:161], a[224:231], v210
	v_smfmac_f32_16x16x64_f16 v[234:237], v[158:161], v[122:129], v210
	v_smfmac_f32_16x16x64_f16 v[238:241], v[130:133], a[16:23], v210
	s_waitcnt lgkmcnt(4)
	v_smfmac_f32_16x16x64_f16 v[242:245], v[130:133], v[180:187], v210
	ds_read_b128 v[180:183], v199 offset:12288
	ds_read_b128 v[184:187], v199 offset:13312
	v_smfmac_f32_16x16x64_f16 v[238:241], v[134:137], a[48:55], v210
	v_fmac_f32_e32 v230, s40, v231
	v_fmac_f32_e32 v234, s40, v235
	s_waitcnt lgkmcnt(4)
	v_smfmac_f32_16x16x64_f16 v[242:245], v[134:137], v[188:195], v210
	ds_read_b128 v[188:191], v199 offset:16384
	ds_read_b128 v[192:195], v199 offset:17408
	v_fmac_f32_e32 v230, s41, v232
	v_fmac_f32_e32 v234, s41, v236
	v_smfmac_f32_16x16x64_f16 v[238:241], v[138:141], a[80:87], v210
	s_nop 0
	v_permlane32_swap_b32_e32 v230, v234
	v_add_f32_e32 v166, v230, v234
	s_waitcnt lgkmcnt(4)
	v_smfmac_f32_16x16x64_f16 v[242:245], v[138:141], v[222:229], v210
	ds_read_b128 v[222:225], v199 offset:20480
	ds_read_b128 v[226:229], v199 offset:21504
	v_fmac_f32_e32 v179, 0x40638e39, v166
	v_fma_mixlo_f16 v232, v178, v179, v171
	v_smfmac_f32_16x16x64_f16 v[238:241], v[142:145], a[112:119], v210
	v_fma_f32 v231, v178, v179, v171
	v_fma_mix_f32 v231, v231, 1.0, -v232 op_sel_hi:[0,0,1]
	s_waitcnt lgkmcnt(4)
	v_smfmac_f32_16x16x64_f16 v[242:245], v[142:145], v[180:187], v210
	ds_read_b128 v[180:183], v199 offset:24576
	ds_read_b128 v[184:187], v199 offset:25600
	v_fma_mixlo_f16 v235, v231, s42, 0
	v_fma_mix_f32 v231, v231, s42, -v235 op_sel_hi:[0,0,1]
	v_smfmac_f32_16x16x64_f16 v[238:241], v[146:149], a[144:151], v210
	v_fma_mixlo_f16 v233, v231, s42, 0
	ds_write_b16 v204, v232
	s_waitcnt lgkmcnt(5)
	v_smfmac_f32_16x16x64_f16 v[242:245], v[146:149], v[188:195], v210
	ds_read_b128 v[188:191], v199 offset:28672
	ds_read_b128 v[192:195], v199 offset:29696
	ds_write_b16 v204, v235 offset:544
	ds_write_b16 v204, v233 offset:1088
	v_smfmac_f32_16x16x64_f16 v[238:241], v[150:153], a[176:183], v210
	v_mov_b64_e32 v[230:231], 0
	v_mov_b64_e32 v[232:233], 0
	s_waitcnt lgkmcnt(7)
	v_smfmac_f32_16x16x64_f16 v[242:245], v[150:153], v[222:229], v210
	ds_read_b128 v[222:225], v199 offset:2048
	ds_read_b128 v[226:229], v199 offset:3072
	v_mov_b64_e32 v[234:235], 0
	v_mov_b64_e32 v[236:237], 0
	v_smfmac_f32_16x16x64_f16 v[238:241], v[154:157], a[208:215], v210
	s_waitcnt lgkmcnt(7)
	v_smfmac_f32_16x16x64_f16 v[242:245], v[154:157], v[180:187], v210
	ds_read_b128 v[180:183], v199 offset:6144
	ds_read_b128 v[184:187], v199 offset:7168
	v_smfmac_f32_16x16x64_f16 v[238:241], v[158:161], a[240:247], v210
	s_waitcnt lgkmcnt(6)
	v_smfmac_f32_16x16x64_f16 v[242:245], v[158:161], v[188:195], v210
	ds_read_b128 v[188:191], v199 offset:10240
	ds_read_b128 v[192:195], v199 offset:11264
	v_smfmac_f32_16x16x64_f16 v[230:233], v[130:133], a[8:15], v210
	v_smfmac_f32_16x16x64_f16 v[234:237], v[130:133], v[2:9], v210
	v_smfmac_f32_16x16x64_f16 v[230:233], v[134:137], a[32:39], v210
	v_fmac_f32_e32 v238, s40, v239
	v_fmac_f32_e32 v242, s40, v243
	v_smfmac_f32_16x16x64_f16 v[234:237], v[134:137], v[10:17], v210
	v_fmac_f32_e32 v238, s41, v240
	v_fmac_f32_e32 v242, s41, v244
	v_smfmac_f32_16x16x64_f16 v[230:233], v[138:141], a[72:79], v210
	s_nop 0
	v_permlane32_swap_b32_e32 v238, v242
	v_add_f32_e32 v176, v238, v242
	v_smfmac_f32_16x16x64_f16 v[234:237], v[138:141], v[50:57], v210
	v_fmac_f32_e32 v197, 0x40638e39, v176
	v_fma_mixlo_f16 v240, v178, v197, v169
	v_smfmac_f32_16x16x64_f16 v[230:233], v[142:145], a[104:111], v210
	v_fma_f32 v239, v178, v197, v169
	v_fma_mix_f32 v239, v239, 1.0, -v240 op_sel_hi:[0,0,1]
	v_smfmac_f32_16x16x64_f16 v[234:237], v[142:145], v[26:33], v210
	v_fma_mixlo_f16 v243, v239, s42, 0
	v_fma_mix_f32 v239, v239, s42, -v243 op_sel_hi:[0,0,1]
	v_smfmac_f32_16x16x64_f16 v[230:233], v[146:149], a[136:143], v210
	v_fma_mixlo_f16 v241, v239, s42, 0
	ds_write_b16 v206, v240
	v_smfmac_f32_16x16x64_f16 v[234:237], v[146:149], v[82:89], v210
	ds_write_b16 v206, v243 offset:544
	ds_write_b16 v206, v241 offset:1088
	v_smfmac_f32_16x16x64_f16 v[230:233], v[150:153], a[168:175], v210
	v_mov_b64_e32 v[238:239], 0
	v_mov_b64_e32 v[240:241], 0
	v_smfmac_f32_16x16x64_f16 v[234:237], v[150:153], v[66:73], v210
	v_mov_b64_e32 v[242:243], 0
	v_mov_b64_e32 v[244:245], 0
	v_smfmac_f32_16x16x64_f16 v[230:233], v[154:157], a[200:207], v210
	v_smfmac_f32_16x16x64_f16 v[234:237], v[154:157], v[114:121], v210
	v_smfmac_f32_16x16x64_f16 v[230:233], v[158:161], a[232:239], v210
	v_smfmac_f32_16x16x64_f16 v[234:237], v[158:161], v[90:97], v210
	v_smfmac_f32_16x16x64_f16 v[238:241], v[130:133], a[24:31], v210
	s_waitcnt lgkmcnt(7)
	v_smfmac_f32_16x16x64_f16 v[242:245], v[130:133], v[222:229], v210
	ds_read_b128 v[222:225], v199 offset:14336
	ds_read_b128 v[226:229], v199 offset:15360
	v_smfmac_f32_16x16x64_f16 v[238:241], v[134:137], a[56:63], v210
	v_fmac_f32_e32 v230, s40, v231
	v_fmac_f32_e32 v234, s40, v235
	s_waitcnt lgkmcnt(7)
	v_smfmac_f32_16x16x64_f16 v[242:245], v[134:137], v[180:187], v210
	ds_read_b128 v[180:183], v199 offset:18432
	ds_read_b128 v[184:187], v199 offset:19456
	v_fmac_f32_e32 v230, s41, v232
	v_fmac_f32_e32 v234, s41, v236
	v_smfmac_f32_16x16x64_f16 v[238:241], v[138:141], a[88:95], v210
	s_nop 0
	v_permlane32_swap_b32_e32 v230, v234
	v_add_f32_e32 v167, v230, v234
	s_waitcnt lgkmcnt(7)
	v_smfmac_f32_16x16x64_f16 v[242:245], v[138:141], v[188:195], v210
	ds_read_b128 v[188:191], v199 offset:22528
	ds_read_b128 v[192:195], v199 offset:23552
	v_fmac_f32_e32 v196, 0x40638e39, v167
	v_fma_mixlo_f16 v232, v178, v196, v170
	v_smfmac_f32_16x16x64_f16 v[238:241], v[142:145], a[120:127], v210
	v_fma_f32 v231, v178, v196, v170
	v_fma_mix_f32 v231, v231, 1.0, -v232 op_sel_hi:[0,0,1]
	s_waitcnt lgkmcnt(4)
	v_smfmac_f32_16x16x64_f16 v[242:245], v[142:145], v[222:229], v210
	ds_read_b128 v[222:225], v199 offset:26624
	ds_read_b128 v[226:229], v199 offset:27648
	v_fma_mixlo_f16 v235, v231, s42, 0
	v_fma_mix_f32 v231, v231, s42, -v235 op_sel_hi:[0,0,1]
	v_smfmac_f32_16x16x64_f16 v[238:241], v[146:149], a[152:159], v210
	v_fma_mixlo_f16 v233, v231, s42, 0
	ds_write_b16 v205, v232
	s_waitcnt lgkmcnt(5)
	v_smfmac_f32_16x16x64_f16 v[242:245], v[146:149], v[180:187], v210
	ds_read_b128 v[180:183], v199 offset:30720
	ds_read_b128 v[184:187], v199 offset:31744
	ds_write_b16 v205, v235 offset:544
	ds_write_b16 v205, v233 offset:1088
	v_smfmac_f32_16x16x64_f16 v[238:241], v[150:153], a[184:191], v210
	v_mov_b64_e32 v[230:231], 0
	v_mov_b64_e32 v[232:233], 0
	s_waitcnt lgkmcnt(7)
	v_smfmac_f32_16x16x64_f16 v[242:245], v[150:153], v[188:195], v210
	v_mov_b64_e32 v[234:235], 0
	v_mov_b64_e32 v[236:237], 0
	v_smfmac_f32_16x16x64_f16 v[238:241], v[154:157], a[216:223], v210
	s_waitcnt lgkmcnt(5)
	v_smfmac_f32_16x16x64_f16 v[242:245], v[154:157], v[222:229], v210
	v_smfmac_f32_16x16x64_f16 v[238:241], v[158:161], a[248:255], v210
	s_waitcnt lgkmcnt(2)
	v_smfmac_f32_16x16x64_f16 v[242:245], v[158:161], v[180:187], v210
	s_nop 5
	v_fmac_f32_e32 v238, s40, v239
	s_nop 0
	v_fmac_f32_e32 v242, s40, v243
	v_fmac_f32_e32 v238, s41, v240
	v_fmac_f32_e32 v242, s41, v244
	s_nop 1
	v_permlane32_swap_b32_e32 v238, v242
	v_add_f32_e32 v177, v238, v242
	v_fmac_f32_e32 v198, 0x40638e39, v177
	v_fma_mixlo_f16 v240, v178, v198, v168
	v_fma_f32 v239, v178, v198, v168
	v_fma_mix_f32 v239, v239, 1.0, -v240 op_sel_hi:[0,0,1]
	v_fma_mixlo_f16 v243, v239, s42, 0
	v_fma_mix_f32 v239, v239, s42, -v243 op_sel_hi:[0,0,1]
	v_fma_mixlo_f16 v241, v239, s42, 0
	ds_write_b16 v207, v240
	ds_write_b16 v207, v243 offset:544
	ds_write_b16 v207, v241 offset:1088
	s_waitcnt lgkmcnt(0)
	s_barrier
	ds_read_b128 v[130:133], v208
	ds_read_b128 v[134:137], v209 offset:64
	ds_read_b128 v[138:141], v211
	ds_read_b128 v[142:145], v212
	ds_read_b128 v[146:149], v213
	ds_read_b128 v[150:153], v214
	ds_read_b128 v[154:157], v215
	ds_read_b128 v[158:161], v216
	ds_read_b128 v[180:183], v199 offset:0
	ds_read_b128 v[184:187], v199 offset:1024
	ds_read_b128 v[188:191], v199 offset:4096
	ds_read_b128 v[192:195], v199 offset:5120
	ds_read_b128 v[222:225], v199 offset:8192
	ds_read_b128 v[226:229], v199 offset:9216
	s_waitcnt lgkmcnt(13)
	v_smfmac_f32_16x16x64_f16 v[230:233], v[130:133], a[0:7], v210
	v_mov_b64_e32 v[238:239], 0
	v_mov_b64_e32 v[240:241], 0
	v_smfmac_f32_16x16x64_f16 v[234:237], v[130:133], v[18:25], v210
	v_mov_b64_e32 v[242:243], 0
	v_mov_b64_e32 v[244:245], 0
	s_waitcnt lgkmcnt(12)
	v_smfmac_f32_16x16x64_f16 v[230:233], v[134:137], a[40:47], v210
	v_mul_f32_e32 v219, 0x403cf760, v173
	v_fmac_f32_e32 v219, 0xc139885f, v162
	v_smfmac_f32_16x16x64_f16 v[234:237], v[134:137], v[34:41], v210
	v_fmac_f32_e32 v219, 0x411d2a92, v166
	v_mul_f32_e32 v220, 0x403cf760, v172
	s_waitcnt lgkmcnt(11)
	v_smfmac_f32_16x16x64_f16 v[230:233], v[138:141], a[64:71], v210
	v_fmac_f32_e32 v220, 0xc139885f, v163
	v_fmac_f32_e32 v220, 0x411d2a92, v167
	v_smfmac_f32_16x16x64_f16 v[234:237], v[138:141], v[42:49], v210
	v_mul_f32_e32 v246, 0x403cf760, v175
	v_fmac_f32_e32 v246, 0xc139885f, v164
	s_waitcnt lgkmcnt(10)
	v_smfmac_f32_16x16x64_f16 v[230:233], v[142:145], a[96:103], v210
	v_fmac_f32_e32 v246, 0x411d2a92, v176
	v_mul_f32_e32 v247, 0x403cf760, v174
	v_smfmac_f32_16x16x64_f16 v[234:237], v[142:145], v[58:65], v210
	v_fmac_f32_e32 v247, 0xc139885f, v165
	v_fmac_f32_e32 v247, 0x411d2a92, v177
	s_waitcnt lgkmcnt(9)
	v_smfmac_f32_16x16x64_f16 v[230:233], v[146:149], a[128:135], v210
	v_smfmac_f32_16x16x64_f16 v[234:237], v[146:149], v[74:81], v210
	s_waitcnt lgkmcnt(8)
	v_smfmac_f32_16x16x64_f16 v[230:233], v[150:153], a[160:167], v210
	v_smfmac_f32_16x16x64_f16 v[234:237], v[150:153], v[98:105], v210
	s_waitcnt lgkmcnt(7)
	v_smfmac_f32_16x16x64_f16 v[230:233], v[154:157], a[192:199], v210
	v_smfmac_f32_16x16x64_f16 v[234:237], v[154:157], v[106:113], v210
	s_waitcnt lgkmcnt(6)
	v_smfmac_f32_16x16x64_f16 v[230:233], v[158:161], a[224:231], v210
	v_smfmac_f32_16x16x64_f16 v[234:237], v[158:161], v[122:129], v210
	v_smfmac_f32_16x16x64_f16 v[238:241], v[130:133], a[16:23], v210
	s_waitcnt lgkmcnt(4)
	v_smfmac_f32_16x16x64_f16 v[242:245], v[130:133], v[180:187], v210
	ds_read_b128 v[180:183], v199 offset:12288
	ds_read_b128 v[184:187], v199 offset:13312
	v_smfmac_f32_16x16x64_f16 v[238:241], v[134:137], a[48:55], v210
	v_fmac_f32_e32 v230, s40, v231
	v_fmac_f32_e32 v234, s40, v235
	s_waitcnt lgkmcnt(4)
	v_smfmac_f32_16x16x64_f16 v[242:245], v[134:137], v[188:195], v210
	ds_read_b128 v[188:191], v199 offset:16384
	ds_read_b128 v[192:195], v199 offset:17408
	v_fmac_f32_e32 v230, s41, v232
	v_fmac_f32_e32 v234, s41, v236
	v_smfmac_f32_16x16x64_f16 v[238:241], v[138:141], a[80:87], v210
	s_nop 0
	v_permlane32_swap_b32_e32 v230, v234
	v_add_f32_e32 v179, v230, v234
	s_waitcnt lgkmcnt(4)
	v_smfmac_f32_16x16x64_f16 v[242:245], v[138:141], v[222:229], v210
	ds_read_b128 v[222:225], v199 offset:20480
	ds_read_b128 v[226:229], v199 offset:21504
	v_fmac_f32_e32 v219, 0xbe94e4f6, v179
	v_fma_mixlo_f16 v232, v178, v219, v171
	v_smfmac_f32_16x16x64_f16 v[238:241], v[142:145], a[112:119], v210
	v_fma_f32 v231, v178, v219, v171
	v_fma_mix_f32 v231, v231, 1.0, -v232 op_sel_hi:[0,0,1]
	s_waitcnt lgkmcnt(4)
	v_smfmac_f32_16x16x64_f16 v[242:245], v[142:145], v[180:187], v210
	ds_read_b128 v[180:183], v199 offset:24576
	ds_read_b128 v[184:187], v199 offset:25600
	v_fma_mixlo_f16 v235, v231, s42, 0
	v_fma_mix_f32 v231, v231, s42, -v235 op_sel_hi:[0,0,1]
	v_smfmac_f32_16x16x64_f16 v[238:241], v[146:149], a[144:151], v210
	v_fma_mixlo_f16 v233, v231, s42, 0
	ds_write_b16 v204, v232 offset:8704
	s_waitcnt lgkmcnt(5)
	v_smfmac_f32_16x16x64_f16 v[242:245], v[146:149], v[188:195], v210
	ds_read_b128 v[188:191], v199 offset:28672
	ds_read_b128 v[192:195], v199 offset:29696
	ds_write_b16 v204, v235 offset:9248
	ds_write_b16 v204, v233 offset:9792
	v_smfmac_f32_16x16x64_f16 v[238:241], v[150:153], a[176:183], v210
	v_mov_b64_e32 v[230:231], 0
	v_mov_b64_e32 v[232:233], 0
	s_waitcnt lgkmcnt(7)
	v_smfmac_f32_16x16x64_f16 v[242:245], v[150:153], v[222:229], v210
	ds_read_b128 v[222:225], v199 offset:2048
	ds_read_b128 v[226:229], v199 offset:3072
	v_mov_b64_e32 v[234:235], 0
	v_mov_b64_e32 v[236:237], 0
	v_smfmac_f32_16x16x64_f16 v[238:241], v[154:157], a[208:215], v210
	s_waitcnt lgkmcnt(7)
	v_smfmac_f32_16x16x64_f16 v[242:245], v[154:157], v[180:187], v210
	ds_read_b128 v[180:183], v199 offset:6144
	ds_read_b128 v[184:187], v199 offset:7168
	v_smfmac_f32_16x16x64_f16 v[238:241], v[158:161], a[240:247], v210
	s_waitcnt lgkmcnt(6)
	v_smfmac_f32_16x16x64_f16 v[242:245], v[158:161], v[188:195], v210
	ds_read_b128 v[188:191], v199 offset:10240
	ds_read_b128 v[192:195], v199 offset:11264
	v_smfmac_f32_16x16x64_f16 v[230:233], v[130:133], a[8:15], v210
	v_smfmac_f32_16x16x64_f16 v[234:237], v[130:133], v[2:9], v210
	v_smfmac_f32_16x16x64_f16 v[230:233], v[134:137], a[32:39], v210
	v_fmac_f32_e32 v238, s40, v239
	v_fmac_f32_e32 v242, s40, v243
	v_smfmac_f32_16x16x64_f16 v[234:237], v[134:137], v[10:17], v210
	v_fmac_f32_e32 v238, s41, v240
	v_fmac_f32_e32 v242, s41, v244
	v_smfmac_f32_16x16x64_f16 v[230:233], v[138:141], a[72:79], v210
	s_nop 0
	v_permlane32_swap_b32_e32 v238, v242
	v_add_f32_e32 v197, v238, v242
	v_smfmac_f32_16x16x64_f16 v[234:237], v[138:141], v[50:57], v210
	v_fmac_f32_e32 v246, 0xbe94e4f6, v197
	v_fma_mixlo_f16 v240, v178, v246, v169
	v_smfmac_f32_16x16x64_f16 v[230:233], v[142:145], a[104:111], v210
	v_fma_f32 v239, v178, v246, v169
	v_fma_mix_f32 v239, v239, 1.0, -v240 op_sel_hi:[0,0,1]
	v_smfmac_f32_16x16x64_f16 v[234:237], v[142:145], v[26:33], v210
	v_fma_mixlo_f16 v243, v239, s42, 0
	v_fma_mix_f32 v239, v239, s42, -v243 op_sel_hi:[0,0,1]
	v_smfmac_f32_16x16x64_f16 v[230:233], v[146:149], a[136:143], v210
	v_fma_mixlo_f16 v241, v239, s42, 0
	ds_write_b16 v206, v240 offset:8704
	v_smfmac_f32_16x16x64_f16 v[234:237], v[146:149], v[82:89], v210
	ds_write_b16 v206, v243 offset:9248
	ds_write_b16 v206, v241 offset:9792
	v_smfmac_f32_16x16x64_f16 v[230:233], v[150:153], a[168:175], v210
	v_mov_b64_e32 v[238:239], 0
	v_mov_b64_e32 v[240:241], 0
	v_smfmac_f32_16x16x64_f16 v[234:237], v[150:153], v[66:73], v210
	v_mov_b64_e32 v[242:243], 0
	v_mov_b64_e32 v[244:245], 0
	v_smfmac_f32_16x16x64_f16 v[230:233], v[154:157], a[200:207], v210
	v_smfmac_f32_16x16x64_f16 v[234:237], v[154:157], v[114:121], v210
	v_smfmac_f32_16x16x64_f16 v[230:233], v[158:161], a[232:239], v210
	v_smfmac_f32_16x16x64_f16 v[234:237], v[158:161], v[90:97], v210
	v_smfmac_f32_16x16x64_f16 v[238:241], v[130:133], a[24:31], v210
	s_waitcnt lgkmcnt(7)
	v_smfmac_f32_16x16x64_f16 v[242:245], v[130:133], v[222:229], v210
	ds_read_b128 v[222:225], v199 offset:14336
	ds_read_b128 v[226:229], v199 offset:15360
	v_smfmac_f32_16x16x64_f16 v[238:241], v[134:137], a[56:63], v210
	v_fmac_f32_e32 v230, s40, v231
	v_fmac_f32_e32 v234, s40, v235
	s_waitcnt lgkmcnt(7)
	v_smfmac_f32_16x16x64_f16 v[242:245], v[134:137], v[180:187], v210
	ds_read_b128 v[180:183], v199 offset:18432
	ds_read_b128 v[184:187], v199 offset:19456
	v_fmac_f32_e32 v230, s41, v232
	v_fmac_f32_e32 v234, s41, v236
	v_smfmac_f32_16x16x64_f16 v[238:241], v[138:141], a[88:95], v210
	s_nop 0
	v_permlane32_swap_b32_e32 v230, v234
	v_add_f32_e32 v196, v230, v234
	s_waitcnt lgkmcnt(7)
	v_smfmac_f32_16x16x64_f16 v[242:245], v[138:141], v[188:195], v210
	ds_read_b128 v[188:191], v199 offset:22528
	ds_read_b128 v[192:195], v199 offset:23552
	v_fmac_f32_e32 v220, 0xbe94e4f6, v196
	v_fma_mixlo_f16 v232, v178, v220, v170
	v_smfmac_f32_16x16x64_f16 v[238:241], v[142:145], a[120:127], v210
	v_fma_f32 v231, v178, v220, v170
	v_fma_mix_f32 v231, v231, 1.0, -v232 op_sel_hi:[0,0,1]
	s_waitcnt lgkmcnt(4)
	v_smfmac_f32_16x16x64_f16 v[242:245], v[142:145], v[222:229], v210
	ds_read_b128 v[222:225], v199 offset:26624
	ds_read_b128 v[226:229], v199 offset:27648
	v_fma_mixlo_f16 v235, v231, s42, 0
	v_fma_mix_f32 v231, v231, s42, -v235 op_sel_hi:[0,0,1]
	v_smfmac_f32_16x16x64_f16 v[238:241], v[146:149], a[152:159], v210
	v_fma_mixlo_f16 v233, v231, s42, 0
	ds_write_b16 v205, v232 offset:8704
	s_waitcnt lgkmcnt(5)
	v_smfmac_f32_16x16x64_f16 v[242:245], v[146:149], v[180:187], v210
	ds_read_b128 v[180:183], v199 offset:30720
	ds_read_b128 v[184:187], v199 offset:31744
	ds_write_b16 v205, v235 offset:9248
	ds_write_b16 v205, v233 offset:9792
	v_smfmac_f32_16x16x64_f16 v[238:241], v[150:153], a[184:191], v210
	v_mov_b64_e32 v[230:231], 0
	v_mov_b64_e32 v[232:233], 0
	s_waitcnt lgkmcnt(7)
	v_smfmac_f32_16x16x64_f16 v[242:245], v[150:153], v[188:195], v210
	v_mov_b64_e32 v[234:235], 0
	v_mov_b64_e32 v[236:237], 0
	v_smfmac_f32_16x16x64_f16 v[238:241], v[154:157], a[216:223], v210
	s_waitcnt lgkmcnt(5)
	v_smfmac_f32_16x16x64_f16 v[242:245], v[154:157], v[222:229], v210
	v_smfmac_f32_16x16x64_f16 v[238:241], v[158:161], a[248:255], v210
	s_waitcnt lgkmcnt(2)
	v_smfmac_f32_16x16x64_f16 v[242:245], v[158:161], v[180:187], v210
	s_nop 5
	v_fmac_f32_e32 v238, s40, v239
	s_nop 0
	v_fmac_f32_e32 v242, s40, v243
	v_fmac_f32_e32 v238, s41, v240
	v_fmac_f32_e32 v242, s41, v244
	s_nop 1
	v_permlane32_swap_b32_e32 v238, v242
	v_add_f32_e32 v198, v238, v242
	v_fmac_f32_e32 v247, 0xbe94e4f6, v198
	v_fma_mixlo_f16 v240, v178, v247, v168
	v_fma_f32 v239, v178, v247, v168
	v_fma_mix_f32 v239, v239, 1.0, -v240 op_sel_hi:[0,0,1]
	v_fma_mixlo_f16 v243, v239, s42, 0
	v_fma_mix_f32 v239, v239, s42, -v243 op_sel_hi:[0,0,1]
	v_fma_mixlo_f16 v241, v239, s42, 0
	ds_write_b16 v207, v240 offset:8704
	ds_write_b16 v207, v243 offset:9248
	ds_write_b16 v207, v241 offset:9792
	s_waitcnt lgkmcnt(0)
	s_barrier
	ds_read_b128 v[130:133], v208 offset:8704
	ds_read_b128 v[134:137], v209 offset:8768
	ds_read_b128 v[138:141], v211 offset:8704
	ds_read_b128 v[142:145], v212 offset:8704
	ds_read_b128 v[146:149], v213 offset:8704
	ds_read_b128 v[150:153], v214 offset:8704
	ds_read_b128 v[154:157], v215 offset:8704
	ds_read_b128 v[158:161], v216 offset:8704
	ds_read_b128 v[180:183], v199 offset:0
	ds_read_b128 v[184:187], v199 offset:1024
	ds_read_b128 v[188:191], v199 offset:4096
	ds_read_b128 v[192:195], v199 offset:5120
	ds_read_b128 v[222:225], v199 offset:8192
	ds_read_b128 v[226:229], v199 offset:9216
	s_waitcnt lgkmcnt(13)
	v_smfmac_f32_16x16x64_f16 v[230:233], v[130:133], a[0:7], v210
	v_mov_b64_e32 v[238:239], 0
	v_mov_b64_e32 v[240:241], 0
	v_smfmac_f32_16x16x64_f16 v[234:237], v[130:133], v[18:25], v210
	v_mov_b64_e32 v[242:243], 0
	v_mov_b64_e32 v[244:245], 0
	s_waitcnt lgkmcnt(12)
	v_smfmac_f32_16x16x64_f16 v[230:233], v[134:137], a[40:47], v210
	v_mul_f32_e32 v248, 0x40362960, v173
	v_fmac_f32_e32 v248, 0xc12c1f08, v162
	v_smfmac_f32_16x16x64_f16 v[234:237], v[134:137], v[34:41], v210
	v_fmac_f32_e32 v248, 0x410e80b5, v166
	v_fmac_f32_e32 v248, 0x3e8e8ba3, v179
	s_waitcnt lgkmcnt(11)
	v_smfmac_f32_16x16x64_f16 v[230:233], v[138:141], a[64:71], v210
	v_mul_f32_e32 v249, 0x40362960, v172
	v_fmac_f32_e32 v249, 0xc12c1f08, v163
	v_smfmac_f32_16x16x64_f16 v[234:237], v[138:141], v[42:49], v210
	v_fmac_f32_e32 v249, 0x410e80b5, v167
	v_fmac_f32_e32 v249, 0x3e8e8ba3, v196
	s_waitcnt lgkmcnt(10)
	v_smfmac_f32_16x16x64_f16 v[230:233], v[142:145], a[96:103], v210
	v_mul_f32_e32 v250, 0x40362960, v175
	v_fmac_f32_e32 v250, 0xc12c1f08, v164
	v_smfmac_f32_16x16x64_f16 v[234:237], v[142:145], v[58:65], v210
	v_fmac_f32_e32 v250, 0x410e80b5, v176
	v_fmac_f32_e32 v250, 0x3e8e8ba3, v197
	s_waitcnt lgkmcnt(9)
	v_smfmac_f32_16x16x64_f16 v[230:233], v[146:149], a[128:135], v210
	v_mul_f32_e32 v251, 0x40362960, v174
	v_fmac_f32_e32 v251, 0xc12c1f08, v165
	v_smfmac_f32_16x16x64_f16 v[234:237], v[146:149], v[74:81], v210
	v_fmac_f32_e32 v251, 0x410e80b5, v177
	v_fmac_f32_e32 v251, 0x3e8e8ba3, v198
	s_waitcnt lgkmcnt(8)
	v_smfmac_f32_16x16x64_f16 v[230:233], v[150:153], a[160:167], v210
	v_smfmac_f32_16x16x64_f16 v[234:237], v[150:153], v[98:105], v210
	s_waitcnt lgkmcnt(7)
	v_smfmac_f32_16x16x64_f16 v[230:233], v[154:157], a[192:199], v210
	v_smfmac_f32_16x16x64_f16 v[234:237], v[154:157], v[106:113], v210
	s_waitcnt lgkmcnt(6)
	v_smfmac_f32_16x16x64_f16 v[230:233], v[158:161], a[224:231], v210
	v_smfmac_f32_16x16x64_f16 v[234:237], v[158:161], v[122:129], v210
	v_smfmac_f32_16x16x64_f16 v[238:241], v[130:133], a[16:23], v210
	s_waitcnt lgkmcnt(4)
	v_smfmac_f32_16x16x64_f16 v[242:245], v[130:133], v[180:187], v210
	ds_read_b128 v[180:183], v199 offset:12288
	ds_read_b128 v[184:187], v199 offset:13312
	v_smfmac_f32_16x16x64_f16 v[238:241], v[134:137], a[48:55], v210
	v_fmac_f32_e32 v230, s40, v231
	v_fmac_f32_e32 v234, s40, v235
	s_waitcnt lgkmcnt(4)
	v_smfmac_f32_16x16x64_f16 v[242:245], v[134:137], v[188:195], v210
	ds_read_b128 v[188:191], v199 offset:16384
	ds_read_b128 v[192:195], v199 offset:17408
	v_fmac_f32_e32 v230, s41, v232
	v_fmac_f32_e32 v234, s41, v236
	v_smfmac_f32_16x16x64_f16 v[238:241], v[138:141], a[80:87], v210
	s_nop 0
	v_permlane32_swap_b32_e32 v230, v234
	v_add_f32_e32 v219, v230, v234
	s_waitcnt lgkmcnt(4)
	v_smfmac_f32_16x16x64_f16 v[242:245], v[138:141], v[222:229], v210
	ds_read_b128 v[222:225], v199 offset:20480
	ds_read_b128 v[226:229], v199 offset:21504
	v_fmac_f32_e32 v248, 0xbe8c0c4c, v219
	v_fma_mixlo_f16 v232, v178, v248, v171
	v_smfmac_f32_16x16x64_f16 v[238:241], v[142:145], a[112:119], v210
	v_fma_f32 v231, v178, v248, v171
	v_fma_mix_f32 v231, v231, 1.0, -v232 op_sel_hi:[0,0,1]
	s_waitcnt lgkmcnt(4)
	v_smfmac_f32_16x16x64_f16 v[242:245], v[142:145], v[180:187], v210
	ds_read_b128 v[180:183], v199 offset:24576
	ds_read_b128 v[184:187], v199 offset:25600
	v_fma_mixlo_f16 v235, v231, s42, 0
	v_fma_mix_f32 v231, v231, s42, -v235 op_sel_hi:[0,0,1]
	v_smfmac_f32_16x16x64_f16 v[238:241], v[146:149], a[144:151], v210
	v_fma_mixlo_f16 v233, v231, s42, 0
	ds_write_b16 v204, v232
	s_waitcnt lgkmcnt(5)
	v_smfmac_f32_16x16x64_f16 v[242:245], v[146:149], v[188:195], v210
	ds_read_b128 v[188:191], v199 offset:28672
	ds_read_b128 v[192:195], v199 offset:29696
	ds_write_b16 v204, v235 offset:544
	ds_write_b16 v204, v233 offset:1088
	v_smfmac_f32_16x16x64_f16 v[238:241], v[150:153], a[176:183], v210
	v_mov_b64_e32 v[230:231], 0
	v_mov_b64_e32 v[232:233], 0
	s_waitcnt lgkmcnt(7)
	v_smfmac_f32_16x16x64_f16 v[242:245], v[150:153], v[222:229], v210
	ds_read_b128 v[222:225], v199 offset:2048
	ds_read_b128 v[226:229], v199 offset:3072
	v_mov_b64_e32 v[234:235], 0
	v_mov_b64_e32 v[236:237], 0
	v_smfmac_f32_16x16x64_f16 v[238:241], v[154:157], a[208:215], v210
	s_waitcnt lgkmcnt(7)
	v_smfmac_f32_16x16x64_f16 v[242:245], v[154:157], v[180:187], v210
	ds_read_b128 v[180:183], v199 offset:6144
	ds_read_b128 v[184:187], v199 offset:7168
	v_smfmac_f32_16x16x64_f16 v[238:241], v[158:161], a[240:247], v210
	s_waitcnt lgkmcnt(6)
	v_smfmac_f32_16x16x64_f16 v[242:245], v[158:161], v[188:195], v210
	ds_read_b128 v[188:191], v199 offset:10240
	ds_read_b128 v[192:195], v199 offset:11264
	v_smfmac_f32_16x16x64_f16 v[230:233], v[130:133], a[8:15], v210
	v_smfmac_f32_16x16x64_f16 v[234:237], v[130:133], v[2:9], v210
	v_smfmac_f32_16x16x64_f16 v[230:233], v[134:137], a[32:39], v210
	v_fmac_f32_e32 v238, s40, v239
	v_fmac_f32_e32 v242, s40, v243
	v_smfmac_f32_16x16x64_f16 v[234:237], v[134:137], v[10:17], v210
	v_fmac_f32_e32 v238, s41, v240
	v_fmac_f32_e32 v242, s41, v244
	v_smfmac_f32_16x16x64_f16 v[230:233], v[138:141], a[72:79], v210
	s_nop 0
	v_permlane32_swap_b32_e32 v238, v242
	v_add_f32_e32 v246, v238, v242
	v_smfmac_f32_16x16x64_f16 v[234:237], v[138:141], v[50:57], v210
	v_fmac_f32_e32 v250, 0xbe8c0c4c, v246
	v_fma_mixlo_f16 v240, v178, v250, v169
	v_smfmac_f32_16x16x64_f16 v[230:233], v[142:145], a[104:111], v210
	v_fma_f32 v239, v178, v250, v169
	v_fma_mix_f32 v239, v239, 1.0, -v240 op_sel_hi:[0,0,1]
	v_smfmac_f32_16x16x64_f16 v[234:237], v[142:145], v[26:33], v210
	v_fma_mixlo_f16 v243, v239, s42, 0
	v_fma_mix_f32 v239, v239, s42, -v243 op_sel_hi:[0,0,1]
	v_smfmac_f32_16x16x64_f16 v[230:233], v[146:149], a[136:143], v210
	v_fma_mixlo_f16 v241, v239, s42, 0
	ds_write_b16 v206, v240
	v_smfmac_f32_16x16x64_f16 v[234:237], v[146:149], v[82:89], v210
	ds_write_b16 v206, v243 offset:544
	ds_write_b16 v206, v241 offset:1088
	v_smfmac_f32_16x16x64_f16 v[230:233], v[150:153], a[168:175], v210
	v_mov_b64_e32 v[238:239], 0
	v_mov_b64_e32 v[240:241], 0
	v_smfmac_f32_16x16x64_f16 v[234:237], v[150:153], v[66:73], v210
	v_mov_b64_e32 v[242:243], 0
	v_mov_b64_e32 v[244:245], 0
	v_smfmac_f32_16x16x64_f16 v[230:233], v[154:157], a[200:207], v210
	v_smfmac_f32_16x16x64_f16 v[234:237], v[154:157], v[114:121], v210
	v_smfmac_f32_16x16x64_f16 v[230:233], v[158:161], a[232:239], v210
	v_smfmac_f32_16x16x64_f16 v[234:237], v[158:161], v[90:97], v210
	v_smfmac_f32_16x16x64_f16 v[238:241], v[130:133], a[24:31], v210
	s_waitcnt lgkmcnt(7)
	v_smfmac_f32_16x16x64_f16 v[242:245], v[130:133], v[222:229], v210
	ds_read_b128 v[222:225], v199 offset:14336
	ds_read_b128 v[226:229], v199 offset:15360
	v_smfmac_f32_16x16x64_f16 v[238:241], v[134:137], a[56:63], v210
	v_fmac_f32_e32 v230, s40, v231
	v_fmac_f32_e32 v234, s40, v235
	s_waitcnt lgkmcnt(7)
	v_smfmac_f32_16x16x64_f16 v[242:245], v[134:137], v[180:187], v210
	ds_read_b128 v[180:183], v199 offset:18432
	ds_read_b128 v[184:187], v199 offset:19456
	v_fmac_f32_e32 v230, s41, v232
	v_fmac_f32_e32 v234, s41, v236
	v_smfmac_f32_16x16x64_f16 v[238:241], v[138:141], a[88:95], v210
	s_nop 0
	v_permlane32_swap_b32_e32 v230, v234
	v_add_f32_e32 v220, v230, v234
	s_waitcnt lgkmcnt(7)
	v_smfmac_f32_16x16x64_f16 v[242:245], v[138:141], v[188:195], v210
	ds_read_b128 v[188:191], v199 offset:22528
	ds_read_b128 v[192:195], v199 offset:23552
	v_fmac_f32_e32 v249, 0xbe8c0c4c, v220
	v_fma_mixlo_f16 v232, v178, v249, v170
	v_smfmac_f32_16x16x64_f16 v[238:241], v[142:145], a[120:127], v210
	v_fma_f32 v231, v178, v249, v170
	v_fma_mix_f32 v231, v231, 1.0, -v232 op_sel_hi:[0,0,1]
	s_waitcnt lgkmcnt(4)
	v_smfmac_f32_16x16x64_f16 v[242:245], v[142:145], v[222:229], v210
	ds_read_b128 v[222:225], v199 offset:26624
	ds_read_b128 v[226:229], v199 offset:27648
	v_fma_mixlo_f16 v235, v231, s42, 0
	v_fma_mix_f32 v231, v231, s42, -v235 op_sel_hi:[0,0,1]
	v_smfmac_f32_16x16x64_f16 v[238:241], v[146:149], a[152:159], v210
	v_fma_mixlo_f16 v233, v231, s42, 0
	ds_write_b16 v205, v232
	s_waitcnt lgkmcnt(5)
	v_smfmac_f32_16x16x64_f16 v[242:245], v[146:149], v[180:187], v210
	ds_read_b128 v[180:183], v199 offset:30720
	ds_read_b128 v[184:187], v199 offset:31744
	ds_write_b16 v205, v235 offset:544
	ds_write_b16 v205, v233 offset:1088
	v_smfmac_f32_16x16x64_f16 v[238:241], v[150:153], a[184:191], v210
	v_mov_b64_e32 v[230:231], 0
	v_mov_b64_e32 v[232:233], 0
	s_waitcnt lgkmcnt(7)
	v_smfmac_f32_16x16x64_f16 v[242:245], v[150:153], v[188:195], v210
	v_mov_b64_e32 v[234:235], 0
	v_mov_b64_e32 v[236:237], 0
	v_smfmac_f32_16x16x64_f16 v[238:241], v[154:157], a[216:223], v210
	s_waitcnt lgkmcnt(5)
	v_smfmac_f32_16x16x64_f16 v[242:245], v[154:157], v[222:229], v210
	v_smfmac_f32_16x16x64_f16 v[238:241], v[158:161], a[248:255], v210
	s_waitcnt lgkmcnt(2)
	v_smfmac_f32_16x16x64_f16 v[242:245], v[158:161], v[180:187], v210
	s_nop 5
	v_fmac_f32_e32 v238, s40, v239
	s_nop 0
	v_fmac_f32_e32 v242, s40, v243
	v_fmac_f32_e32 v238, s41, v240
	v_fmac_f32_e32 v242, s41, v244
	s_nop 1
	v_permlane32_swap_b32_e32 v238, v242
	v_add_f32_e32 v247, v238, v242
	v_fmac_f32_e32 v251, 0xbe8c0c4c, v247
	v_fma_mixlo_f16 v240, v178, v251, v168
	v_fma_f32 v239, v178, v251, v168
	v_fma_mix_f32 v239, v239, 1.0, -v240 op_sel_hi:[0,0,1]
	v_fma_mixlo_f16 v243, v239, s42, 0
	v_fma_mix_f32 v239, v239, s42, -v243 op_sel_hi:[0,0,1]
	v_fma_mixlo_f16 v241, v239, s42, 0
	ds_write_b16 v207, v240
	ds_write_b16 v207, v243 offset:544
	ds_write_b16 v207, v241 offset:1088
	s_waitcnt lgkmcnt(0)
	s_barrier
	ds_read_b128 v[130:133], v208
	ds_read_b128 v[134:137], v209 offset:64
	ds_read_b128 v[138:141], v211
	ds_read_b128 v[142:145], v212
	ds_read_b128 v[146:149], v213
	ds_read_b128 v[150:153], v214
	ds_read_b128 v[154:157], v215
	ds_read_b128 v[158:161], v216
	ds_read_b128 v[180:183], v199 offset:0
	ds_read_b128 v[184:187], v199 offset:1024
	ds_read_b128 v[188:191], v199 offset:4096
	ds_read_b128 v[192:195], v199 offset:5120
	ds_read_b128 v[222:225], v199 offset:8192
	ds_read_b128 v[226:229], v199 offset:9216
	s_waitcnt lgkmcnt(13)
	v_smfmac_f32_16x16x64_f16 v[230:233], v[130:133], a[0:7], v210
	v_mov_b64_e32 v[238:239], 0
	v_mov_b64_e32 v[240:241], 0
	v_smfmac_f32_16x16x64_f16 v[234:237], v[130:133], v[18:25], v210
	v_mov_b64_e32 v[242:243], 0
	v_mov_b64_e32 v[244:245], 0
	s_waitcnt lgkmcnt(12)
	v_smfmac_f32_16x16x64_f16 v[230:233], v[134:137], a[40:47], v210
	v_mul_f32_e32 v252, 0x3dbaaaab, v173
	v_fmac_f32_e32 v252, 0x3ee6024d, v166
	v_smfmac_f32_16x16x64_f16 v[234:237], v[134:137], v[34:41], v210
	v_fmac_f32_e32 v252, 0x3f26aaab, v179
	v_fmac_f32_e32 v252, 0xbea50e7e, v219
	s_waitcnt lgkmcnt(11)
	v_smfmac_f32_16x16x64_f16 v[230:233], v[138:141], a[64:71], v210
	v_mul_f32_e32 v253, 0x3dbaaaab, v172
	v_fmac_f32_e32 v253, 0x3ee6024d, v167
	v_smfmac_f32_16x16x64_f16 v[234:237], v[138:141], v[42:49], v210
	v_fmac_f32_e32 v253, 0x3f26aaab, v196
	v_fmac_f32_e32 v253, 0xbea50e7e, v220
	s_waitcnt lgkmcnt(10)
	v_smfmac_f32_16x16x64_f16 v[230:233], v[142:145], a[96:103], v210
	v_mul_f32_e32 v254, 0x3dbaaaab, v175
	v_fmac_f32_e32 v254, 0x3ee6024d, v176
	v_smfmac_f32_16x16x64_f16 v[234:237], v[142:145], v[58:65], v210
	v_fmac_f32_e32 v254, 0x3f26aaab, v197
	v_fmac_f32_e32 v254, 0xbea50e7e, v246
	s_waitcnt lgkmcnt(9)
	v_smfmac_f32_16x16x64_f16 v[230:233], v[146:149], a[128:135], v210
	v_mul_f32_e32 v255, 0x3dbaaaab, v174
	v_fmac_f32_e32 v255, 0x3ee6024d, v177
	v_smfmac_f32_16x16x64_f16 v[234:237], v[146:149], v[74:81], v210
	v_fmac_f32_e32 v255, 0x3f26aaab, v198
	v_fmac_f32_e32 v255, 0xbea50e7e, v247
	s_waitcnt lgkmcnt(8)
	v_smfmac_f32_16x16x64_f16 v[230:233], v[150:153], a[160:167], v210
	v_smfmac_f32_16x16x64_f16 v[234:237], v[150:153], v[98:105], v210
	s_waitcnt lgkmcnt(7)
	v_smfmac_f32_16x16x64_f16 v[230:233], v[154:157], a[192:199], v210
	v_smfmac_f32_16x16x64_f16 v[234:237], v[154:157], v[106:113], v210
	s_waitcnt lgkmcnt(6)
	v_smfmac_f32_16x16x64_f16 v[230:233], v[158:161], a[224:231], v210
	v_smfmac_f32_16x16x64_f16 v[234:237], v[158:161], v[122:129], v210
	v_smfmac_f32_16x16x64_f16 v[238:241], v[130:133], a[16:23], v210
	s_waitcnt lgkmcnt(4)
	v_smfmac_f32_16x16x64_f16 v[242:245], v[130:133], v[180:187], v210
	ds_read_b128 v[180:183], v199 offset:12288
	ds_read_b128 v[184:187], v199 offset:13312
	v_smfmac_f32_16x16x64_f16 v[238:241], v[134:137], a[48:55], v210
	v_fmac_f32_e32 v230, s40, v231
	v_fmac_f32_e32 v234, s40, v235
	s_waitcnt lgkmcnt(4)
	v_smfmac_f32_16x16x64_f16 v[242:245], v[134:137], v[188:195], v210
	ds_read_b128 v[188:191], v199 offset:16384
	ds_read_b128 v[192:195], v199 offset:17408
	v_fmac_f32_e32 v230, s41, v232
	v_fmac_f32_e32 v234, s41, v236
	v_smfmac_f32_16x16x64_f16 v[238:241], v[138:141], a[80:87], v210
	s_nop 0
	v_permlane32_swap_b32_e32 v230, v234
	v_add_f32_e32 v248, v230, v234
	s_waitcnt lgkmcnt(4)
	v_smfmac_f32_16x16x64_f16 v[242:245], v[138:141], v[222:229], v210
	ds_read_b128 v[222:225], v199 offset:20480
	ds_read_b128 v[226:229], v199 offset:21504
	v_fmac_f32_e32 v252, 0x3e061862, v248
	v_mov_b32_e32 v236, v252
	v_smfmac_f32_16x16x64_f16 v[238:241], v[142:145], a[112:119], v210
	v_fma_mixlo_f16 v232, v178, v236, v171
	v_fma_f32 v252, v178, v236, v171
	s_waitcnt lgkmcnt(4)
	v_smfmac_f32_16x16x64_f16 v[242:245], v[142:145], v[180:187], v210
	ds_read_b128 v[180:183], v199 offset:24576
	ds_read_b128 v[184:187], v199 offset:25600
	v_fma_mix_f32 v231, v252, 1.0, -v232 op_sel_hi:[0,0,1]
	v_fma_mixlo_f16 v235, v231, s42, 0
	v_smfmac_f32_16x16x64_f16 v[238:241], v[146:149], a[144:151], v210
	v_fma_mix_f32 v231, v231, s42, -v235 op_sel_hi:[0,0,1]
	v_fma_mixlo_f16 v233, v231, s42, 0
	s_waitcnt lgkmcnt(4)
	v_smfmac_f32_16x16x64_f16 v[242:245], v[146:149], v[188:195], v210
	ds_read_b128 v[188:191], v199 offset:28672
	ds_read_b128 v[192:195], v199 offset:29696
	ds_write_b16 v204, v232 offset:8704
	ds_write_b16 v204, v235 offset:9248
	v_smfmac_f32_16x16x64_f16 v[238:241], v[150:153], a[176:183], v210
	ds_write_b16 v204, v233 offset:9792
	v_mov_b64_e32 v[230:231], 0
	s_waitcnt lgkmcnt(7)
	v_smfmac_f32_16x16x64_f16 v[242:245], v[150:153], v[222:229], v210
	ds_read_b128 v[222:225], v199 offset:2048
	ds_read_b128 v[226:229], v199 offset:3072
	v_mov_b64_e32 v[232:233], 0
	v_mov_b64_e32 v[234:235], 0
	v_smfmac_f32_16x16x64_f16 v[238:241], v[154:157], a[208:215], v210
	v_mov_b64_e32 v[236:237], 0
	s_waitcnt lgkmcnt(7)
	v_smfmac_f32_16x16x64_f16 v[242:245], v[154:157], v[180:187], v210
	ds_read_b128 v[180:183], v199 offset:6144
	ds_read_b128 v[184:187], v199 offset:7168
	v_smfmac_f32_16x16x64_f16 v[238:241], v[158:161], a[240:247], v210
	s_waitcnt lgkmcnt(7)
	v_smfmac_f32_16x16x64_f16 v[242:245], v[158:161], v[188:195], v210
	ds_read_b128 v[188:191], v199 offset:10240
	ds_read_b128 v[192:195], v199 offset:11264
	v_smfmac_f32_16x16x64_f16 v[230:233], v[130:133], a[8:15], v210
	v_smfmac_f32_16x16x64_f16 v[234:237], v[130:133], v[2:9], v210
	v_smfmac_f32_16x16x64_f16 v[230:233], v[134:137], a[32:39], v210
	v_fmac_f32_e32 v238, s40, v239
	v_fmac_f32_e32 v242, s40, v243
	v_smfmac_f32_16x16x64_f16 v[234:237], v[134:137], v[10:17], v210
	v_fmac_f32_e32 v238, s41, v240
	v_fmac_f32_e32 v242, s41, v244
	v_smfmac_f32_16x16x64_f16 v[230:233], v[138:141], a[72:79], v210
	s_nop 0
	v_permlane32_swap_b32_e32 v238, v242
	v_add_f32_e32 v250, v238, v242
	v_smfmac_f32_16x16x64_f16 v[234:237], v[138:141], v[50:57], v210
	v_fmac_f32_e32 v254, 0x3e061862, v250
	v_mov_b32_e32 v244, v254
	v_smfmac_f32_16x16x64_f16 v[230:233], v[142:145], a[104:111], v210
	v_fma_mixlo_f16 v240, v178, v244, v169
	v_fma_f32 v254, v178, v244, v169
	v_smfmac_f32_16x16x64_f16 v[234:237], v[142:145], v[26:33], v210
	v_fma_mix_f32 v239, v254, 1.0, -v240 op_sel_hi:[0,0,1]
	v_fma_mixlo_f16 v243, v239, s42, 0
	v_smfmac_f32_16x16x64_f16 v[230:233], v[146:149], a[136:143], v210
	v_fma_mix_f32 v239, v239, s42, -v243 op_sel_hi:[0,0,1]
	v_fma_mixlo_f16 v241, v239, s42, 0
	v_smfmac_f32_16x16x64_f16 v[234:237], v[146:149], v[82:89], v210
	ds_write_b16 v206, v240 offset:8704
	ds_write_b16 v206, v243 offset:9248
	v_smfmac_f32_16x16x64_f16 v[230:233], v[150:153], a[168:175], v210
	ds_write_b16 v206, v241 offset:9792
	v_mov_b64_e32 v[238:239], 0
	v_smfmac_f32_16x16x64_f16 v[234:237], v[150:153], v[66:73], v210
	v_mov_b64_e32 v[240:241], 0
	v_mov_b64_e32 v[242:243], 0
	v_smfmac_f32_16x16x64_f16 v[230:233], v[154:157], a[200:207], v210
	v_mov_b64_e32 v[244:245], 0
	v_smfmac_f32_16x16x64_f16 v[234:237], v[154:157], v[114:121], v210
	v_smfmac_f32_16x16x64_f16 v[230:233], v[158:161], a[232:239], v210
	v_smfmac_f32_16x16x64_f16 v[234:237], v[158:161], v[90:97], v210
	v_smfmac_f32_16x16x64_f16 v[238:241], v[130:133], a[24:31], v210
	s_waitcnt lgkmcnt(7)
	v_smfmac_f32_16x16x64_f16 v[242:245], v[130:133], v[222:229], v210
	ds_read_b128 v[222:225], v199 offset:14336
	ds_read_b128 v[226:229], v199 offset:15360
	v_smfmac_f32_16x16x64_f16 v[238:241], v[134:137], a[56:63], v210
	v_fmac_f32_e32 v230, s40, v231
	v_fmac_f32_e32 v234, s40, v235
	s_waitcnt lgkmcnt(7)
	v_smfmac_f32_16x16x64_f16 v[242:245], v[134:137], v[180:187], v210
	ds_read_b128 v[180:183], v199 offset:18432
	ds_read_b128 v[184:187], v199 offset:19456
	v_fmac_f32_e32 v230, s41, v232
	v_fmac_f32_e32 v234, s41, v236
	v_smfmac_f32_16x16x64_f16 v[238:241], v[138:141], a[88:95], v210
	s_nop 0
	v_permlane32_swap_b32_e32 v230, v234
	v_add_f32_e32 v249, v230, v234
	s_waitcnt lgkmcnt(7)
	v_smfmac_f32_16x16x64_f16 v[242:245], v[138:141], v[188:195], v210
	ds_read_b128 v[188:191], v199 offset:22528
	ds_read_b128 v[192:195], v199 offset:23552
	v_fmac_f32_e32 v253, 0x3e061862, v249
	v_mov_b32_e32 v236, v253
	v_smfmac_f32_16x16x64_f16 v[238:241], v[142:145], a[120:127], v210
	v_fma_mixlo_f16 v232, v178, v236, v170
	v_fma_f32 v253, v178, v236, v170
	s_waitcnt lgkmcnt(4)
	v_smfmac_f32_16x16x64_f16 v[242:245], v[142:145], v[222:229], v210
	ds_read_b128 v[222:225], v199 offset:26624
	ds_read_b128 v[226:229], v199 offset:27648
	v_fma_mix_f32 v231, v253, 1.0, -v232 op_sel_hi:[0,0,1]
	v_fma_mixlo_f16 v235, v231, s42, 0
	v_smfmac_f32_16x16x64_f16 v[238:241], v[146:149], a[152:159], v210
	v_fma_mix_f32 v231, v231, s42, -v235 op_sel_hi:[0,0,1]
	v_fma_mixlo_f16 v233, v231, s42, 0
	s_waitcnt lgkmcnt(4)
	v_smfmac_f32_16x16x64_f16 v[242:245], v[146:149], v[180:187], v210
	ds_read_b128 v[180:183], v199 offset:30720
	ds_read_b128 v[184:187], v199 offset:31744
	ds_write_b16 v205, v232 offset:8704
	ds_write_b16 v205, v235 offset:9248
	v_smfmac_f32_16x16x64_f16 v[238:241], v[150:153], a[184:191], v210
	ds_write_b16 v205, v233 offset:9792
	v_mov_b64_e32 v[230:231], 0
	s_waitcnt lgkmcnt(7)
	v_smfmac_f32_16x16x64_f16 v[242:245], v[150:153], v[188:195], v210
	v_mov_b64_e32 v[232:233], 0
	v_mov_b64_e32 v[234:235], 0
	v_smfmac_f32_16x16x64_f16 v[238:241], v[154:157], a[216:223], v210
	v_mov_b64_e32 v[236:237], 0
	s_waitcnt lgkmcnt(5)
	v_smfmac_f32_16x16x64_f16 v[242:245], v[154:157], v[222:229], v210
	v_smfmac_f32_16x16x64_f16 v[238:241], v[158:161], a[248:255], v210
	s_waitcnt lgkmcnt(3)
	v_smfmac_f32_16x16x64_f16 v[242:245], v[158:161], v[180:187], v210
	s_nop 5
	v_fmac_f32_e32 v238, s40, v239
	s_nop 0
	v_fmac_f32_e32 v242, s40, v243
	v_fmac_f32_e32 v238, s41, v240
	v_fmac_f32_e32 v242, s41, v244
	s_nop 1
	v_permlane32_swap_b32_e32 v238, v242
	v_add_f32_e32 v251, v238, v242
	v_fmac_f32_e32 v255, 0x3e061862, v251
	v_mov_b32_e32 v244, v255
	v_fma_mixlo_f16 v240, v178, v244, v168
	v_fma_f32 v255, v178, v244, v168
	v_fma_mix_f32 v239, v255, 1.0, -v240 op_sel_hi:[0,0,1]
	v_fma_mixlo_f16 v243, v239, s42, 0
	v_fma_mix_f32 v239, v239, s42, -v243 op_sel_hi:[0,0,1]
	v_fma_mixlo_f16 v241, v239, s42, 0
	ds_write_b16 v207, v240 offset:8704
	ds_write_b16 v207, v243 offset:9248
	ds_write_b16 v207, v241 offset:9792
	s_waitcnt lgkmcnt(0)
	s_barrier
	ds_read_b128 v[130:133], v208 offset:8704
	ds_read_b128 v[134:137], v209 offset:8768
	ds_read_b128 v[138:141], v211 offset:8704
	ds_read_b128 v[142:145], v212 offset:8704
	ds_read_b128 v[146:149], v213 offset:8704
	ds_read_b128 v[150:153], v214 offset:8704
	ds_read_b128 v[154:157], v215 offset:8704
	ds_read_b128 v[158:161], v216 offset:8704
	ds_read_b128 v[180:183], v199 offset:0
	ds_read_b128 v[184:187], v199 offset:1024
	ds_read_b128 v[188:191], v199 offset:4096
	ds_read_b128 v[192:195], v199 offset:5120
	ds_read_b128 v[222:225], v199 offset:8192
	ds_read_b128 v[226:229], v199 offset:9216
	s_waitcnt lgkmcnt(13)
	v_smfmac_f32_16x16x64_f16 v[230:233], v[130:133], a[0:7], v210
	v_mov_b64_e32 v[238:239], 0
	v_mov_b64_e32 v[240:241], 0
	v_smfmac_f32_16x16x64_f16 v[234:237], v[130:133], v[18:25], v210
	v_mov_b64_e32 v[242:243], 0
	v_mov_b64_e32 v[244:245], 0
	s_waitcnt lgkmcnt(12)
	v_smfmac_f32_16x16x64_f16 v[230:233], v[134:137], a[40:47], v210
	v_mul_f32_e32 v162, 0x3aa1907f, v173
	v_fmac_f32_e32 v162, 0xbb8b5ad3, v166
	v_smfmac_f32_16x16x64_f16 v[234:237], v[134:137], v[34:41], v210
	v_fmac_f32_e32 v162, 0x3d177777, v179
	v_fmac_f32_e32 v162, 0xbd50568f, v219
	s_waitcnt lgkmcnt(11)
	v_smfmac_f32_16x16x64_f16 v[230:233], v[138:141], a[64:71], v210
	v_fmac_f32_e32 v162, 0x3d2ba454, v248
	v_mul_f32_e32 v163, 0x3aa1907f, v172
	v_smfmac_f32_16x16x64_f16 v[234:237], v[138:141], v[42:49], v210
	v_fmac_f32_e32 v163, 0xbb8b5ad3, v167
	v_fmac_f32_e32 v163, 0x3d177777, v196
	s_waitcnt lgkmcnt(10)
	v_smfmac_f32_16x16x64_f16 v[230:233], v[142:145], a[96:103], v210
	v_fmac_f32_e32 v163, 0xbd50568f, v220
	v_fmac_f32_e32 v163, 0x3d2ba454, v249
	v_smfmac_f32_16x16x64_f16 v[234:237], v[142:145], v[58:65], v210
	v_mul_f32_e32 v164, 0x3aa1907f, v175
	v_fmac_f32_e32 v164, 0xbb8b5ad3, v176
	s_waitcnt lgkmcnt(9)
	v_smfmac_f32_16x16x64_f16 v[230:233], v[146:149], a[128:135], v210
	v_fmac_f32_e32 v164, 0x3d177777, v197
	v_fmac_f32_e32 v164, 0xbd50568f, v246
	v_smfmac_f32_16x16x64_f16 v[234:237], v[146:149], v[74:81], v210
	v_fmac_f32_e32 v164, 0x3d2ba454, v250
	v_mul_f32_e32 v165, 0x3aa1907f, v174
	s_waitcnt lgkmcnt(8)
	v_smfmac_f32_16x16x64_f16 v[230:233], v[150:153], a[160:167], v210
	v_fmac_f32_e32 v165, 0xbb8b5ad3, v177
	v_fmac_f32_e32 v165, 0x3d177777, v198
	v_smfmac_f32_16x16x64_f16 v[234:237], v[150:153], v[98:105], v210
	v_fmac_f32_e32 v165, 0xbd50568f, v247
	v_fmac_f32_e32 v165, 0x3d2ba454, v251
	s_waitcnt lgkmcnt(7)
	v_smfmac_f32_16x16x64_f16 v[230:233], v[154:157], a[192:199], v210
	v_max_f32_e64 v179, |v171|, |v252|
	v_mov_b32_e32 v248, 0x358637bd
	v_smfmac_f32_16x16x64_f16 v[234:237], v[154:157], v[106:113], v210
	v_fmac_f32_e32 v248, 0x3a83126f, v179
	v_rcp_f32_e32 v179, v248
	s_waitcnt lgkmcnt(6)
	v_smfmac_f32_16x16x64_f16 v[230:233], v[158:161], a[224:231], v210
	v_max_f32_e64 v196, |v170|, |v253|
	v_mov_b32_e32 v249, 0x358637bd
	v_smfmac_f32_16x16x64_f16 v[234:237], v[158:161], v[122:129], v210
	v_fmac_f32_e32 v249, 0x3a83126f, v196
	v_rcp_f32_e32 v196, v249
	v_max_f32_e64 v197, |v169|, |v254|
	v_mov_b32_e32 v250, 0x358637bd
	v_fmac_f32_e32 v250, 0x3a83126f, v197
	v_rcp_f32_e32 v197, v250
	v_max_f32_e64 v198, |v168|, |v255|
	v_mov_b32_e32 v251, 0x358637bd
	v_fmac_f32_e32 v251, 0x3a83126f, v198
	v_rcp_f32_e32 v198, v251
	v_smfmac_f32_16x16x64_f16 v[238:241], v[130:133], a[16:23], v210
	s_waitcnt lgkmcnt(4)
	v_smfmac_f32_16x16x64_f16 v[242:245], v[130:133], v[180:187], v210
	ds_read_b128 v[180:183], v199 offset:12288
	ds_read_b128 v[184:187], v199 offset:13312
	v_smfmac_f32_16x16x64_f16 v[238:241], v[134:137], a[48:55], v210
	v_fmac_f32_e32 v230, s40, v231
	v_fmac_f32_e32 v234, s40, v235
	s_waitcnt lgkmcnt(4)
	v_smfmac_f32_16x16x64_f16 v[242:245], v[134:137], v[188:195], v210
	ds_read_b128 v[188:191], v199 offset:16384
	ds_read_b128 v[192:195], v199 offset:17408
	v_fmac_f32_e32 v230, s41, v232
	v_fmac_f32_e32 v234, s41, v236
	v_smfmac_f32_16x16x64_f16 v[238:241], v[138:141], a[80:87], v210
	s_nop 0
	v_permlane32_swap_b32_e32 v230, v234
	v_add_f32_e32 v166, v230, v234
	s_waitcnt lgkmcnt(4)
	v_smfmac_f32_16x16x64_f16 v[242:245], v[138:141], v[222:229], v210
	ds_read_b128 v[222:225], v199 offset:20480
	ds_read_b128 v[226:229], v199 offset:21504
	v_fmac_f32_e32 v162, 0xbccccccd, v166
	v_mul_f32_e32 v231, v178, v162
	v_smfmac_f32_16x16x64_f16 v[238:241], v[142:145], a[112:119], v210
	v_mul_f32_e32 v231, v231, v179
	v_mul_f32_e32 v219, v231, v231
	s_waitcnt lgkmcnt(4)
	v_smfmac_f32_16x16x64_f16 v[242:245], v[142:145], v[180:187], v210
	ds_read_b128 v[180:183], v199 offset:24576
	ds_read_b128 v[184:187], v199 offset:25600
	v_mov_b64_e32 v[230:231], 0
	v_mov_b64_e32 v[232:233], 0
	v_smfmac_f32_16x16x64_f16 v[238:241], v[146:149], a[144:151], v210
	v_mov_b64_e32 v[234:235], 0
	v_mov_b64_e32 v[236:237], 0
	s_waitcnt lgkmcnt(4)
	v_smfmac_f32_16x16x64_f16 v[242:245], v[146:149], v[188:195], v210
	ds_read_b128 v[188:191], v199 offset:28672
	ds_read_b128 v[192:195], v199 offset:29696
	v_smfmac_f32_16x16x64_f16 v[238:241], v[150:153], a[176:183], v210
	s_waitcnt lgkmcnt(4)
	v_smfmac_f32_16x16x64_f16 v[242:245], v[150:153], v[222:229], v210
	ds_read_b128 v[222:225], v199 offset:2048
	ds_read_b128 v[226:229], v199 offset:3072
	v_smfmac_f32_16x16x64_f16 v[238:241], v[154:157], a[208:215], v210
	s_waitcnt lgkmcnt(4)
	v_smfmac_f32_16x16x64_f16 v[242:245], v[154:157], v[180:187], v210
	ds_read_b128 v[180:183], v199 offset:6144
	ds_read_b128 v[184:187], v199 offset:7168
	v_smfmac_f32_16x16x64_f16 v[238:241], v[158:161], a[240:247], v210
	s_waitcnt lgkmcnt(4)
	v_smfmac_f32_16x16x64_f16 v[242:245], v[158:161], v[188:195], v210
	ds_read_b128 v[188:191], v199 offset:10240
	ds_read_b128 v[192:195], v199 offset:11264
	v_smfmac_f32_16x16x64_f16 v[230:233], v[130:133], a[8:15], v210
	v_smfmac_f32_16x16x64_f16 v[234:237], v[130:133], v[2:9], v210
	v_smfmac_f32_16x16x64_f16 v[230:233], v[134:137], a[32:39], v210
	v_fmac_f32_e32 v238, s40, v239
	v_fmac_f32_e32 v242, s40, v243
	v_smfmac_f32_16x16x64_f16 v[234:237], v[134:137], v[10:17], v210
	v_fmac_f32_e32 v238, s41, v240
	v_fmac_f32_e32 v242, s41, v244
	v_smfmac_f32_16x16x64_f16 v[230:233], v[138:141], a[72:79], v210
	s_nop 0
	v_permlane32_swap_b32_e32 v238, v242
	v_add_f32_e32 v176, v238, v242
	v_smfmac_f32_16x16x64_f16 v[234:237], v[138:141], v[50:57], v210
	v_fmac_f32_e32 v164, 0xbccccccd, v176
	v_mul_f32_e32 v239, v178, v164
	v_smfmac_f32_16x16x64_f16 v[230:233], v[142:145], a[104:111], v210
	v_mul_f32_e32 v239, v239, v197
	v_fmac_f32_e32 v219, v239, v239
	v_smfmac_f32_16x16x64_f16 v[234:237], v[142:145], v[26:33], v210
	v_mov_b64_e32 v[238:239], 0
	v_mov_b64_e32 v[240:241], 0
	v_smfmac_f32_16x16x64_f16 v[230:233], v[146:149], a[136:143], v210
	v_mov_b64_e32 v[242:243], 0
	v_mov_b64_e32 v[244:245], 0
	v_smfmac_f32_16x16x64_f16 v[234:237], v[146:149], v[82:89], v210
	v_smfmac_f32_16x16x64_f16 v[230:233], v[150:153], a[168:175], v210
	v_smfmac_f32_16x16x64_f16 v[234:237], v[150:153], v[66:73], v210
	v_smfmac_f32_16x16x64_f16 v[230:233], v[154:157], a[200:207], v210
	v_smfmac_f32_16x16x64_f16 v[234:237], v[154:157], v[114:121], v210
	v_smfmac_f32_16x16x64_f16 v[230:233], v[158:161], a[232:239], v210
	v_smfmac_f32_16x16x64_f16 v[234:237], v[158:161], v[90:97], v210
	v_smfmac_f32_16x16x64_f16 v[238:241], v[130:133], a[24:31], v210
	s_waitcnt lgkmcnt(4)
	v_smfmac_f32_16x16x64_f16 v[242:245], v[130:133], v[222:229], v210
	ds_read_b128 v[222:225], v199 offset:14336
	ds_read_b128 v[226:229], v199 offset:15360
	v_smfmac_f32_16x16x64_f16 v[238:241], v[134:137], a[56:63], v210
	v_fmac_f32_e32 v230, s40, v231
	v_fmac_f32_e32 v234, s40, v235
	s_waitcnt lgkmcnt(4)
	v_smfmac_f32_16x16x64_f16 v[242:245], v[134:137], v[180:187], v210
	ds_read_b128 v[180:183], v199 offset:18432
	ds_read_b128 v[184:187], v199 offset:19456
	v_fmac_f32_e32 v230, s41, v232
	v_fmac_f32_e32 v234, s41, v236
	v_smfmac_f32_16x16x64_f16 v[238:241], v[138:141], a[88:95], v210
	s_nop 0
	v_permlane32_swap_b32_e32 v230, v234
	v_add_f32_e32 v167, v230, v234
	s_waitcnt lgkmcnt(4)
	v_smfmac_f32_16x16x64_f16 v[242:245], v[138:141], v[188:195], v210
	ds_read_b128 v[188:191], v199 offset:22528
	ds_read_b128 v[192:195], v199 offset:23552
	v_fmac_f32_e32 v163, 0xbccccccd, v167
	v_mul_f32_e32 v231, v178, v163
	v_smfmac_f32_16x16x64_f16 v[238:241], v[142:145], a[120:127], v210
	v_mul_f32_e32 v231, v231, v196
	v_fmac_f32_e32 v219, v231, v231
	s_waitcnt lgkmcnt(4)
	v_smfmac_f32_16x16x64_f16 v[242:245], v[142:145], v[222:229], v210
	ds_read_b128 v[222:225], v199 offset:26624
	ds_read_b128 v[226:229], v199 offset:27648
	v_mov_b64_e32 v[230:231], 0
	v_mov_b64_e32 v[232:233], 0
	v_smfmac_f32_16x16x64_f16 v[238:241], v[146:149], a[152:159], v210
	v_mov_b64_e32 v[234:235], 0
	v_mov_b64_e32 v[236:237], 0
	s_waitcnt lgkmcnt(4)
	v_smfmac_f32_16x16x64_f16 v[242:245], v[146:149], v[180:187], v210
	ds_read_b128 v[180:183], v199 offset:30720
	ds_read_b128 v[184:187], v199 offset:31744
	v_smfmac_f32_16x16x64_f16 v[238:241], v[150:153], a[184:191], v210
	s_waitcnt lgkmcnt(4)
	v_smfmac_f32_16x16x64_f16 v[242:245], v[150:153], v[188:195], v210
	v_smfmac_f32_16x16x64_f16 v[238:241], v[154:157], a[216:223], v210
	s_waitcnt lgkmcnt(2)
	v_smfmac_f32_16x16x64_f16 v[242:245], v[154:157], v[222:229], v210
	v_smfmac_f32_16x16x64_f16 v[238:241], v[158:161], a[248:255], v210
	s_waitcnt lgkmcnt(0)
	v_smfmac_f32_16x16x64_f16 v[242:245], v[158:161], v[180:187], v210
	s_nop 5
	v_fmac_f32_e32 v238, s40, v239
	s_nop 0
	v_fmac_f32_e32 v242, s40, v243
	v_fmac_f32_e32 v238, s41, v240
	v_fmac_f32_e32 v242, s41, v244
	s_nop 1
	v_permlane32_swap_b32_e32 v238, v242
	v_add_f32_e32 v177, v238, v242
	v_fmac_f32_e32 v165, 0xbccccccd, v177
	v_mul_f32_e32 v239, v178, v165
	v_mul_f32_e32 v239, v239, v198
	v_fmac_f32_e32 v219, v239, v239
	s_nop 1
	v_add_f32_dpp v238, v219, v219 quad_perm:[1,0,3,2] row_mask:0xf bank_mask:0xf bound_ctrl:1
	s_nop 1
	v_add_f32_dpp v238, v238, v238 quad_perm:[2,3,0,1] row_mask:0xf bank_mask:0xf bound_ctrl:1
	s_nop 1
	v_add_f32_dpp v238, v238, v238 row_half_mirror row_mask:0xf bank_mask:0xf bound_ctrl:1
	s_nop 1
	v_add_f32_dpp v238, v238, v238 row_mirror row_mask:0xf bank_mask:0xf bound_ctrl:1
	v_mov_b32_e32 v239, v238
	s_nop 1
	v_permlane32_swap_b32_e32 v238, v239
	v_add_f32_e32 v238, v238, v239
	v_lshl_add_u32 v240, s29, 6, v218
	v_lshl_add_u32 v241, s29, 6, v217
	s_and_saveexec_b64 s[2:3], s[4:5]
	ds_write_b32 v240, v238
	s_or_b64 exec, exec, s[2:3]
	s_waitcnt lgkmcnt(0)
	s_barrier
	ds_read2_b32 v[130:131], v241 offset1:4
	ds_read2_b32 v[132:133], v241 offset0:8 offset1:12
	s_waitcnt lgkmcnt(1)
	v_add_f32_e32 v238, v130, v131
	s_waitcnt lgkmcnt(0)
	v_add_f32_e32 v238, v238, v132
	v_add_f32_e32 v238, v238, v133
	v_mul_f32_e32 v238, 0x3b000000, v238
	v_max_f32_e32 v238, 0xda24260, v238
	v_sqrt_f32_e32 v238, v238
	s_nop 0
	v_cmp_ngt_f32_e64 s[2:3], 1.0, v238
	v_cmp_gt_f32_e32 vcc, 1.0, v238
	v_log_f32_e32 v239, v238
	v_mul_f32_e32 v241, 0x44000000, v178
	s_and_saveexec_b64 s[26:27], vcc
	v_add_f32_e32 v221, v221, v241
	v_mov_b32_e32 v171, v252
	v_mov_b32_e32 v173, v166
	v_mov_b32_e32 v170, v253
	v_mov_b32_e32 v172, v167
	v_mov_b32_e32 v169, v254
	v_mov_b32_e32 v175, v176
	v_mov_b32_e32 v168, v255
	v_mov_b32_e32 v174, v177
	s_or_b64 exec, exec, s[26:27]
	v_mov_b32_e32 v240, 0x41200000
	s_nop 0
	v_cndmask_b32_e64 v240, v240, 1.0, s[22:23]
	s_xor_b32 s29, s29, 1
	s_add_i32 s30, s30, 1
	v_mul_f32_e32 v239, 0xbe4ccccd, v239
	v_exp_f32_e32 v239, v239
	s_nop 0
	v_mul_f32_e32 v239, 0x3f666666, v239
	v_min_f32_e32 v240, v239, v240
	v_max_f32_e32 v239, 0x3e4ccccd, v239
	v_cndmask_b32_e64 v239, v240, v239, s[2:3]
	v_mul_f32_e32 v1, v241, v239
	s_mov_b64 s[22:23], s[2:3]
	s_branch .Lrk_top
